# attention row-max chains: compiler's s_nop 0 pads after hand-written v_max3 removed (no VALU->VALU hazard)
# baseline (speedup 1.0000x reference)
.LBB0_498:
	v_max3_f32 v2, v16, v206, v17
	v_max3_f32 v158, v207, v212, v214
	v_max3_f32 v159, v141, v145, v141
	v_max3_f32 v2, v2, v213, v215
	v_max3_f32 v158, v158, v208, v210
	v_max3_f32 v2, v2, v209, v211
	v_max3_f32 v158, v158, v216, v218
	v_max3_f32 v2, v2, v217, v219
	v_max3_f32 v158, v158, v154, v138
	v_max3_f32 v2, v2, v155, v139
	v_max3_f32 v158, v158, v220, v222
	v_max3_f32 v2, v2, v221, v223
	v_max3_f32 v158, v158, v156, v142
	v_max3_f32 v2, v2, v157, v143
	v_max3_f32 v158, v158, v140, v144
	v_max3_f32 v2, v2, v158, v159
	v_mov_b32_e32 v158, v2
	s_nop 1
	v_permlane32_swap_b32_e32 v2, v158
	v_max3_f32 v2, v2, v158, v158
	v_cmp_lt_f32_e32 vcc, s47, v2
	s_cbranch_vccz .LBB0_502
	v_max3_f32 v2, v2, v3, v3
	v_exp_f32_e64 v82, -v2
	s_and_saveexec_b64 s[26:27], s[2:3]
	ds_write_b32 v231, v82
	s_or_b64 exec, exec, s[26:27]
	s_waitcnt lgkmcnt(0)
	ds_read_b128 v[84:87], v228 offset:64
	ds_read_b128 v[88:91], v228 offset:96
	ds_read_b128 v[92:95], v228
	ds_read_b128 v[158:161], v228 offset:32
	v_add_f32_e32 v241, v241, v2
	s_waitcnt lgkmcnt(0)
	v_sub_f32_e32 v97, v233, v241
	v_pk_add_f32 v[16:17], v[16:17], v[2:3] op_sel_hi:[1,0] neg_lo:[0,1] neg_hi:[0,1]
	v_pk_add_f32 v[206:207], v[206:207], v[2:3] op_sel_hi:[1,0] neg_lo:[0,1] neg_hi:[0,1]
	v_pk_add_f32 v[212:213], v[212:213], v[2:3] op_sel_hi:[1,0] neg_lo:[0,1] neg_hi:[0,1]
	v_pk_add_f32 v[214:215], v[214:215], v[2:3] op_sel_hi:[1,0] neg_lo:[0,1] neg_hi:[0,1]
	v_pk_add_f32 v[208:209], v[208:209], v[2:3] op_sel_hi:[1,0] neg_lo:[0,1] neg_hi:[0,1]
	v_pk_add_f32 v[210:211], v[210:211], v[2:3] op_sel_hi:[1,0] neg_lo:[0,1] neg_hi:[0,1]
	v_pk_add_f32 v[216:217], v[216:217], v[2:3] op_sel_hi:[1,0] neg_lo:[0,1] neg_hi:[0,1]
	v_pk_add_f32 v[218:219], v[218:219], v[2:3] op_sel_hi:[1,0] neg_lo:[0,1] neg_hi:[0,1]
	v_pk_add_f32 v[154:155], v[154:155], v[2:3] op_sel_hi:[1,0] neg_lo:[0,1] neg_hi:[0,1]
	v_pk_add_f32 v[138:139], v[138:139], v[2:3] op_sel_hi:[1,0] neg_lo:[0,1] neg_hi:[0,1]
	v_pk_add_f32 v[220:221], v[220:221], v[2:3] op_sel_hi:[1,0] neg_lo:[0,1] neg_hi:[0,1]
	v_pk_add_f32 v[222:223], v[222:223], v[2:3] op_sel_hi:[1,0] neg_lo:[0,1] neg_hi:[0,1]
	v_pk_add_f32 v[156:157], v[156:157], v[2:3] op_sel_hi:[1,0] neg_lo:[0,1] neg_hi:[0,1]
	v_pk_add_f32 v[142:143], v[142:143], v[2:3] op_sel_hi:[1,0] neg_lo:[0,1] neg_hi:[0,1]
	v_pk_add_f32 v[140:141], v[140:141], v[2:3] op_sel_hi:[1,0] neg_lo:[0,1] neg_hi:[0,1]
	v_pk_add_f32 v[144:145], v[144:145], v[2:3] op_sel_hi:[1,0] neg_lo:[0,1] neg_hi:[0,1]
	v_mul_f32_e32 v204, v204, v82
	s_waitcnt lgkmcnt(0)
	v_pk_mul_f32 v[80:81], v[80:81], v[90:91]
	v_pk_mul_f32 v[76:77], v[76:77], v[86:87]
	v_pk_mul_f32 v[72:73], v[72:73], v[160:161]
	v_pk_mul_f32 v[68:69], v[68:69], v[94:95]
	v_pk_mul_f32 v[78:79], v[78:79], v[88:89]
	v_pk_mul_f32 v[74:75], v[74:75], v[84:85]
	v_pk_mul_f32 v[70:71], v[70:71], v[158:159]
	v_pk_mul_f32 v[66:67], v[66:67], v[92:93]
	v_pk_mul_f32 v[64:65], v[64:65], v[90:91]
	v_pk_mul_f32 v[60:61], v[60:61], v[86:87]
	v_pk_mul_f32 v[56:57], v[56:57], v[160:161]
	v_pk_mul_f32 v[52:53], v[52:53], v[94:95]
	v_pk_mul_f32 v[62:63], v[62:63], v[88:89]
	v_pk_mul_f32 v[58:59], v[58:59], v[84:85]
	v_pk_mul_f32 v[54:55], v[54:55], v[158:159]
	v_pk_mul_f32 v[50:51], v[50:51], v[92:93]
	v_mov_b32_e32 v96, v97
	v_mov_b32_e32 v95, v97
	v_mov_b32_e32 v94, v97
	v_mov_b32_e32 v93, v97
	v_mov_b32_e32 v92, v97
	v_mov_b32_e32 v91, v97
	v_mov_b32_e32 v90, v97
	v_mov_b32_e32 v89, v97
	v_mov_b32_e32 v88, v97
	v_mov_b32_e32 v87, v97
	v_mov_b32_e32 v86, v97
	v_mov_b32_e32 v85, v97
	v_mov_b32_e32 v84, v97
	v_mov_b32_e32 v83, v97
	v_mov_b32_e32 v82, v97

.LBB0_504:
	v_max3_f32 v2, v158, v160, v159
	v_max3_f32 v106, v161, v114, v224
	v_max3_f32 v107, v99, v9, v99
	v_max3_f32 v2, v2, v115, v225
	v_max3_f32 v106, v106, v116, v118
	v_max3_f32 v2, v2, v117, v119
	v_max3_f32 v106, v106, v102, v104
	v_max3_f32 v2, v2, v103, v105
	v_max3_f32 v106, v106, v100, v10
	v_max3_f32 v2, v2, v101, v11
	v_max3_f32 v106, v106, v14, v6
	v_max3_f32 v2, v2, v15, v7
	v_max3_f32 v106, v106, v12, v4
	v_max3_f32 v2, v2, v13, v5
	v_max3_f32 v106, v106, v98, v8
	v_max3_f32 v2, v2, v106, v107
	v_mov_b32_e32 v106, v2
	s_nop 1
	v_permlane32_swap_b32_e32 v2, v106
	v_max3_f32 v2, v2, v106, v106
	v_cmp_lt_f32_e32 vcc, s47, v2
	s_cbranch_vccz .LBB0_489
	v_max3_f32 v2, v2, v3, v3
	v_exp_f32_e64 v106, -v2
	s_and_saveexec_b64 s[26:27], s[2:3]
	s_cbranch_execz .LBB0_488
	ds_write_b32 v231, v106
	s_branch .LBB0_488

.LBB0_531:
	s_nop 0
	v_max3_f32 v2, v146, v130, v147
	v_max3_f32 v4, v131, v148, v132
	v_max3_f32 v5, v161, v145, v161
	v_max3_f32 v2, v2, v149, v133
	v_max3_f32 v4, v4, v150, v134
	v_max3_f32 v2, v2, v151, v135
	v_max3_f32 v4, v4, v152, v136
	v_max3_f32 v2, v2, v153, v137
	v_max3_f32 v4, v4, v154, v138
	v_max3_f32 v2, v2, v155, v139
	v_max3_f32 v4, v4, v156, v140
	v_max3_f32 v2, v2, v157, v141
	v_max3_f32 v4, v4, v158, v142
	v_max3_f32 v2, v2, v159, v143
	v_max3_f32 v4, v4, v160, v144
	v_max3_f32 v2, v2, v4, v5
	v_mov_b32_e32 v4, v2
	s_nop 1
	v_permlane32_swap_b32_e32 v2, v4
	v_max3_f32 v2, v2, v4, v4
	v_cmp_lt_f32_e32 vcc, s26, v2
	s_cbranch_vccz .LBB0_535
	v_max3_f32 v2, v2, v3, v3
	v_exp_f32_e64 v4, -v2
	s_and_saveexec_b64 s[16:17], s[2:3]
	ds_write_b32 v200, v4
	s_or_b64 exec, exec, s[16:17]
	s_waitcnt lgkmcnt(0)
	ds_read_b128 v[6:9], v199 offset:64
	ds_read_b128 v[10:13], v199 offset:96
	ds_read_b128 v[14:17], v199
	ds_read_b128 v[82:85], v199 offset:32
	v_add_f32_e32 v211, v211, v2
	s_waitcnt lgkmcnt(0)
	v_xor_b32_e32 v97, 0x80000000, v211
	v_pk_add_f32 v[146:147], v[146:147], v[2:3] op_sel_hi:[1,0] neg_lo:[0,1] neg_hi:[0,1]
	v_pk_add_f32 v[130:131], v[130:131], v[2:3] op_sel_hi:[1,0] neg_lo:[0,1] neg_hi:[0,1]
	v_pk_add_f32 v[148:149], v[148:149], v[2:3] op_sel_hi:[1,0] neg_lo:[0,1] neg_hi:[0,1]
	v_pk_add_f32 v[132:133], v[132:133], v[2:3] op_sel_hi:[1,0] neg_lo:[0,1] neg_hi:[0,1]
	v_pk_add_f32 v[150:151], v[150:151], v[2:3] op_sel_hi:[1,0] neg_lo:[0,1] neg_hi:[0,1]
	v_pk_add_f32 v[134:135], v[134:135], v[2:3] op_sel_hi:[1,0] neg_lo:[0,1] neg_hi:[0,1]
	v_pk_add_f32 v[152:153], v[152:153], v[2:3] op_sel_hi:[1,0] neg_lo:[0,1] neg_hi:[0,1]
	v_pk_add_f32 v[136:137], v[136:137], v[2:3] op_sel_hi:[1,0] neg_lo:[0,1] neg_hi:[0,1]
	v_pk_add_f32 v[154:155], v[154:155], v[2:3] op_sel_hi:[1,0] neg_lo:[0,1] neg_hi:[0,1]
	v_pk_add_f32 v[138:139], v[138:139], v[2:3] op_sel_hi:[1,0] neg_lo:[0,1] neg_hi:[0,1]
	v_pk_add_f32 v[156:157], v[156:157], v[2:3] op_sel_hi:[1,0] neg_lo:[0,1] neg_hi:[0,1]
	v_pk_add_f32 v[140:141], v[140:141], v[2:3] op_sel_hi:[1,0] neg_lo:[0,1] neg_hi:[0,1]
	v_pk_add_f32 v[158:159], v[158:159], v[2:3] op_sel_hi:[1,0] neg_lo:[0,1] neg_hi:[0,1]
	v_pk_add_f32 v[142:143], v[142:143], v[2:3] op_sel_hi:[1,0] neg_lo:[0,1] neg_hi:[0,1]
	v_pk_add_f32 v[160:161], v[160:161], v[2:3] op_sel_hi:[1,0] neg_lo:[0,1] neg_hi:[0,1]
	v_pk_add_f32 v[144:145], v[144:145], v[2:3] op_sel_hi:[1,0] neg_lo:[0,1] neg_hi:[0,1]
	v_mul_f32_e32 v210, v210, v4
	s_waitcnt lgkmcnt(0)
	v_pk_mul_f32 v[80:81], v[80:81], v[12:13]
	v_pk_mul_f32 v[76:77], v[76:77], v[8:9]
	v_pk_mul_f32 v[72:73], v[72:73], v[84:85]
	v_pk_mul_f32 v[68:69], v[68:69], v[16:17]
	v_pk_mul_f32 v[78:79], v[78:79], v[10:11]
	v_pk_mul_f32 v[74:75], v[74:75], v[6:7]
	v_pk_mul_f32 v[70:71], v[70:71], v[82:83]
	v_pk_mul_f32 v[66:67], v[66:67], v[14:15]
	v_pk_mul_f32 v[64:65], v[64:65], v[12:13]
	v_pk_mul_f32 v[60:61], v[60:61], v[8:9]
	v_pk_mul_f32 v[56:57], v[56:57], v[84:85]
	v_pk_mul_f32 v[52:53], v[52:53], v[16:17]
	v_pk_mul_f32 v[62:63], v[62:63], v[10:11]
	v_pk_mul_f32 v[58:59], v[58:59], v[6:7]
	v_pk_mul_f32 v[54:55], v[54:55], v[82:83]
	v_pk_mul_f32 v[50:51], v[50:51], v[14:15]
	v_mov_b32_e32 v96, v97
	v_mov_b32_e32 v95, v97
	v_mov_b32_e32 v94, v97
	v_mov_b32_e32 v93, v97
	v_mov_b32_e32 v92, v97
	v_mov_b32_e32 v91, v97
	v_mov_b32_e32 v90, v97
	v_mov_b32_e32 v89, v97
	v_mov_b32_e32 v88, v97
	v_mov_b32_e32 v87, v97
	v_mov_b32_e32 v86, v97
	v_mov_b32_e32 v85, v97
	v_mov_b32_e32 v84, v97
	v_mov_b32_e32 v83, v97
	v_mov_b32_e32 v82, v97

.LBB0_539:
	s_nop 0
	v_max3_f32 v2, v114, v98, v115
	v_max3_f32 v4, v99, v116, v100
	v_max3_f32 v5, v129, v113, v129
	v_max3_f32 v2, v2, v117, v101
	v_max3_f32 v4, v4, v118, v102
	v_max3_f32 v2, v2, v119, v103
	v_max3_f32 v4, v4, v120, v104
	v_max3_f32 v2, v2, v121, v105
	v_max3_f32 v4, v4, v122, v106
	v_max3_f32 v2, v2, v123, v107
	v_max3_f32 v4, v4, v124, v108
	v_max3_f32 v2, v2, v125, v109
	v_max3_f32 v4, v4, v126, v110
	v_max3_f32 v2, v2, v127, v111
	v_max3_f32 v4, v4, v128, v112
	v_max3_f32 v2, v2, v4, v5
	v_mov_b32_e32 v4, v2
	s_nop 1
	v_permlane32_swap_b32_e32 v2, v4
	v_max3_f32 v2, v2, v4, v4
	v_cmp_lt_f32_e32 vcc, s26, v2
	s_cbranch_vccz .LBB0_522
	v_max3_f32 v2, v2, v3, v3
	v_exp_f32_e64 v4, -v2
	s_and_saveexec_b64 s[16:17], s[2:3]
	s_cbranch_execz .LBB0_521
	ds_write_b32 v200, v4
	s_branch .LBB0_521

.LBB0_553:
	s_or_b64 exec, exec, s[10:11]
	v_mov_b32_e32 v2, s25
	s_waitcnt lgkmcnt(0)
	s_barrier
	ds_read_b32 v2, v2
	s_mov_b64 s[10:11], -1
	s_waitcnt lgkmcnt(0)
	v_readfirstlane_b32 s14, v2
	s_cmp_ge_i32 s14, s18
	s_cbranch_scc1 .LBB0_548
	s_add_i32 s10, s14, 0xfffffc00
	s_cmpk_gt_i32 s14, 0x3ff
	s_cselect_b32 s33, s10, s14
	s_ashr_i32 s10, s33, 6
	s_ashr_i32 s11, s10, 31
	s_bfe_u32 s14, s33, 0x10005
	v_readfirstlane_b32 s31, v0
	s_lshl_b64 s[16:17], s[10:11], 11
	s_lshl_b32 s10, s10, 1
	s_and_b32 s30, s33, 31
	s_lshr_b32 s39, s31, 6
	s_lshl_b32 s38, s14, 2
	s_or_b32 s14, s10, s14
	s_lshl_b32 s34, s30, 6
	s_lshl_b32 s35, s39, 3
	s_ashr_i32 s15, s14, 31
	s_add_i32 s29, s35, s34
	s_lshl_b64 s[10:11], s[14:15], 14
	s_add_u32 s40, s19, s10
	s_addc_u32 s41, s20, s11
	s_add_u32 s42, s21, s10
	s_addc_u32 s43, s22, s11
	s_lshl_b32 s10, s39, 4
	s_add_u32 s10, s40, s10
	s_addc_u32 s11, s41, 0
	s_lshr_b32 s31, s31, 2
	v_or_b32_e32 v76, s29, v67
	v_and_or_b32 v14, s31, 48, v71
	s_and_b32 s31, s31, 0x3fffffc0
	v_lshl_add_u64 v[2:3], s[16:17], 0, v[76:77]
	s_add_u32 s40, s42, s31
	v_or_b32_e32 v4, s38, v69
	v_lshlrev_b64 v[2:3], 10, v[2:3]
	s_addc_u32 s41, s43, 0
	v_mov_b32_e32 v89, v77
	v_mov_b32_e32 v91, v77
	v_lshl_add_u64 v[2:3], s[12:13], 0, v[2:3]
	v_lshlrev_b32_e32 v4, 7, v4
	v_mov_b32_e32 v5, v77
	v_lshl_add_u64 v[10:11], s[40:41], 0, v[88:89]
	v_lshl_add_u64 v[12:13], s[10:11], 0, v[90:91]
	v_lshlrev_b32_e32 v14, 7, v14
	v_mov_b32_e32 v15, v77
	v_lshl_add_u64 v[2:3], v[2:3], 0, v[4:5]
	v_mov_b32_e32 v87, v77
	v_lshl_add_u64 v[18:19], v[10:11], 0, v[14:15]
	v_add_co_u32_e32 v14, vcc, s26, v12
	v_lshl_add_u64 v[6:7], v[2:3], 0, v[86:87]
	s_nop 0
	v_addc_co_u32_e32 v15, vcc, 0, v13, vcc
	global_load_dwordx4 v[2:5], v[6:7], off
	global_load_dwordx4 v[92:95], v[6:7], off offset:32
	global_load_dwordx4 v[182:185], v[6:7], off offset:64
	global_load_dwordx4 v[186:189], v[6:7], off offset:96
	s_barrier
	global_load_dwordx4 v[6:9], v90, s[10:11]
	global_load_dwordx4 v[10:13], v[18:19], off
	s_nop 0
	global_load_dwordx4 v[14:17], v[14:15], off
	v_add_co_u32_e32 v18, vcc, s26, v18
	s_lshl_b32 s31, s39, 10
	s_nop 0
	v_addc_co_u32_e32 v19, vcc, 0, v19, vcc
	global_load_dwordx4 v[18:21], v[18:19], off
	v_add_u32_e32 v22, s31, v73
	v_subrev_co_u32_e64 v76, s[10:11], 31, v76
	v_lshrrev_b32_e32 v87, 4, v76
	v_add_u32_e32 v87, 1, v87
	v_cmp_gt_u32_e32 vcc, s27, v76
	v_mov_b32_e32 v203, v77
	s_waitcnt vmcnt(3)
	ds_write_b128 v22, v[6:9]
	s_waitcnt vmcnt(2)
	ds_write_b128 v22, v[10:13] offset:16384
	s_waitcnt vmcnt(1)
	ds_write_b128 v22, v[14:17] offset:8192
	s_waitcnt vmcnt(0)
	ds_write_b128 v22, v[18:21] offset:24576
	s_waitcnt lgkmcnt(0)
	s_barrier
	ds_read_b128 v[6:9], v177
	ds_read_b128 v[10:13], v177 offset:512
	s_waitcnt lgkmcnt(1)
	v_mfma_f32_32x32x16_bf16 v[50:65], v[6:9], v[2:5], 0
	v_cndmask_b32_e32 v76, v180, v87, vcc
	v_cndmask_b32_e64 v76, v76, 0, s[10:11]
	v_cmp_lt_u32_e32 vcc, v75, v76
	s_waitcnt lgkmcnt(0)
	v_mfma_f32_32x32x16_bf16 v[34:49], v[10:13], v[2:5], 0
	ds_read_b128 v[6:9], v177 offset:8192
	ds_read_b128 v[10:13], v177 offset:8704
	ds_read_b128 v[190:193], v177 offset:2048
	ds_read_b128 v[194:197], v177 offset:2560
	s_waitcnt lgkmcnt(3)
	v_mfma_f32_32x32x16_bf16 v[18:33], v[6:9], v[2:5], 0
	s_waitcnt lgkmcnt(2)
	v_mfma_f32_32x32x16_bf16 v[2:17], v[10:13], v[2:5], 0
	s_waitcnt lgkmcnt(1)
	v_mfma_f32_32x32x16_bf16 v[50:65], v[190:193], v[92:95], v[50:65]
	s_waitcnt lgkmcnt(0)
	v_mfma_f32_32x32x16_bf16 v[34:49], v[194:197], v[92:95], v[34:49]
	ds_read_b128 v[190:193], v177 offset:10240
	ds_read_b128 v[194:197], v177 offset:10752
	s_waitcnt lgkmcnt(1)
	v_mfma_f32_32x32x16_bf16 v[18:33], v[190:193], v[92:95], v[18:33]
	s_waitcnt lgkmcnt(0)
	v_mfma_f32_32x32x16_bf16 v[2:17], v[194:197], v[92:95], v[2:17]
	ds_read_b128 v[92:95], v177 offset:4096
	ds_read_b128 v[190:193], v177 offset:4608
	s_waitcnt lgkmcnt(1)
	v_mfma_f32_32x32x16_bf16 v[50:65], v[92:95], v[182:185], v[50:65]
	s_waitcnt lgkmcnt(0)
	v_mfma_f32_32x32x16_bf16 v[34:49], v[190:193], v[182:185], v[34:49]
	ds_read_b128 v[92:95], v177 offset:12288
	ds_read_b128 v[190:193], v177 offset:12800
	s_waitcnt lgkmcnt(1)
	v_mfma_f32_32x32x16_bf16 v[18:33], v[92:95], v[182:185], v[18:33]
	s_waitcnt lgkmcnt(0)
	v_mfma_f32_32x32x16_bf16 v[2:17], v[190:193], v[182:185], v[2:17]
	ds_read_b128 v[92:95], v177 offset:6144
	ds_read_b128 v[182:185], v177 offset:6656
	s_waitcnt lgkmcnt(1)
	v_mfma_f32_32x32x16_bf16 v[50:65], v[92:95], v[186:189], v[50:65]
	s_waitcnt lgkmcnt(0)
	v_mfma_f32_32x32x16_bf16 v[34:49], v[182:185], v[186:189], v[34:49]
	s_nop 9
	v_cndmask_b32_e32 v50, v178, v50, vcc
	v_cmp_lt_u32_e32 vcc, v81, v76
	ds_read_b128 v[92:95], v177 offset:14336
	ds_read_b128 v[182:185], v177 offset:14848
	v_cndmask_b32_e32 v51, v178, v51, vcc
	v_cmp_lt_u32_e32 vcc, v83, v76
	s_nop 1
	v_cndmask_b32_e32 v52, v178, v52, vcc
	v_cmp_lt_u32_e32 vcc, v85, v76
	s_waitcnt lgkmcnt(1)
	v_mfma_f32_32x32x16_bf16 v[18:33], v[92:95], v[186:189], v[18:33]
	v_cndmask_b32_e32 v53, v178, v53, vcc
	v_cmp_lt_u32_e32 vcc, v98, v76
	s_nop 1
	v_cndmask_b32_e32 v54, v178, v54, vcc
	v_cmp_lt_u32_e32 vcc, v99, v76
	s_waitcnt lgkmcnt(0)
	v_mfma_f32_32x32x16_bf16 v[2:17], v[182:185], v[186:189], v[2:17]
	v_cndmask_b32_e32 v55, v178, v55, vcc
	v_cmp_lt_u32_e32 vcc, v100, v76
	s_nop 1
	v_cndmask_b32_e32 v56, v178, v56, vcc
	v_cmp_lt_u32_e32 vcc, v101, v76
	s_nop 1
	v_cndmask_b32_e32 v57, v178, v57, vcc
	v_cmp_lt_u32_e32 vcc, v102, v76
	s_nop 1
	v_cndmask_b32_e32 v58, v178, v58, vcc
	v_cmp_lt_u32_e32 vcc, v103, v76
	s_nop 1
	v_cndmask_b32_e32 v59, v178, v59, vcc
	v_cmp_lt_u32_e32 vcc, v104, v76
	s_nop 1
	v_cndmask_b32_e32 v60, v178, v60, vcc
	v_cmp_lt_u32_e32 vcc, v105, v76
	s_nop 1
	v_cndmask_b32_e32 v61, v178, v61, vcc
	v_cmp_lt_u32_e32 vcc, v106, v76
	s_nop 1
	v_cndmask_b32_e32 v62, v178, v62, vcc
	v_cmp_lt_u32_e32 vcc, v107, v76
	s_nop 1
	v_cndmask_b32_e32 v63, v178, v63, vcc
	v_cmp_lt_u32_e32 vcc, v108, v76
	s_nop 1
	v_cndmask_b32_e32 v64, v178, v64, vcc
	v_cmp_lt_u32_e32 vcc, v109, v76
	s_nop 1
	v_cndmask_b32_e32 v65, v178, v65, vcc
	v_cmp_lt_u32_e32 vcc, v110, v76
	s_nop 1
	v_cndmask_b32_e32 v34, v178, v34, vcc
	v_cmp_lt_u32_e32 vcc, v111, v76
	s_nop 1
	v_cndmask_b32_e32 v35, v178, v35, vcc
	v_cmp_lt_u32_e32 vcc, v112, v76
	s_nop 1
	v_cndmask_b32_e32 v36, v178, v36, vcc
	v_cmp_lt_u32_e32 vcc, v113, v76
	s_nop 1
	v_cndmask_b32_e32 v37, v178, v37, vcc
	v_cmp_lt_u32_e32 vcc, v114, v76
	s_nop 1
	v_cndmask_b32_e32 v38, v178, v38, vcc
	v_cmp_lt_u32_e32 vcc, v115, v76
	s_nop 1
	v_cndmask_b32_e32 v39, v178, v39, vcc
	v_cmp_lt_u32_e32 vcc, v116, v76
	s_nop 1
	v_cndmask_b32_e32 v40, v178, v40, vcc
	v_cmp_lt_u32_e32 vcc, v117, v76
	s_nop 1
	v_cndmask_b32_e32 v41, v178, v41, vcc
	v_cmp_lt_u32_e32 vcc, v118, v76
	s_nop 1
	v_cndmask_b32_e32 v42, v178, v42, vcc
	v_cmp_lt_u32_e32 vcc, v119, v76
	s_nop 1
	v_cndmask_b32_e32 v43, v178, v43, vcc
	v_cmp_lt_u32_e32 vcc, v120, v76
	s_nop 1
	v_cndmask_b32_e32 v44, v178, v44, vcc
	v_cmp_lt_u32_e32 vcc, v121, v76
	s_nop 1
	v_cndmask_b32_e32 v45, v178, v45, vcc
	v_cmp_lt_u32_e32 vcc, v122, v76
	s_nop 1
	v_cndmask_b32_e32 v46, v178, v46, vcc
	v_cmp_lt_u32_e32 vcc, v123, v76
	s_nop 1
	v_cndmask_b32_e32 v47, v178, v47, vcc
	v_cmp_lt_u32_e32 vcc, v124, v76
	s_nop 1
	v_cndmask_b32_e32 v48, v178, v48, vcc
	v_cmp_lt_u32_e32 vcc, v125, v76
	s_nop 1
	v_cndmask_b32_e32 v49, v178, v49, vcc
	v_cmp_lt_u32_e32 vcc, v126, v76
	s_nop 1
	v_cndmask_b32_e32 v87, v178, v18, vcc
	v_cmp_lt_u32_e32 vcc, v127, v76
	s_nop 1
	v_cndmask_b32_e32 v89, v178, v19, vcc
	v_cmp_lt_u32_e32 vcc, v128, v76
	s_nop 1
	v_cndmask_b32_e32 v91, v178, v20, vcc
	v_cmp_lt_u32_e32 vcc, v129, v76
	s_nop 1
	v_cndmask_b32_e32 v92, v178, v21, vcc
	v_cmp_lt_u32_e32 vcc, v130, v76
	s_nop 1
	v_cndmask_b32_e32 v93, v178, v22, vcc
	v_cmp_lt_u32_e32 vcc, v131, v76
	s_nop 1
	v_cndmask_b32_e32 v94, v178, v23, vcc
	v_cmp_lt_u32_e32 vcc, v132, v76
	s_nop 1
	v_cndmask_b32_e32 v24, v178, v24, vcc
	v_cmp_lt_u32_e32 vcc, v133, v76
	s_nop 1
	v_cndmask_b32_e32 v25, v178, v25, vcc
	v_cmp_lt_u32_e32 vcc, v134, v76
	s_nop 1
	v_cndmask_b32_e32 v26, v178, v26, vcc
	v_cmp_lt_u32_e32 vcc, v135, v76
	s_nop 1
	v_cndmask_b32_e32 v27, v178, v27, vcc
	v_cmp_lt_u32_e32 vcc, v136, v76
	s_nop 1
	v_cndmask_b32_e32 v95, v178, v28, vcc
	v_cmp_lt_u32_e32 vcc, v137, v76
	s_nop 1
	v_cndmask_b32_e32 v96, v178, v29, vcc
	v_cmp_lt_u32_e32 vcc, v138, v76
	s_nop 1
	v_cndmask_b32_e32 v97, v178, v30, vcc
	v_cmp_lt_u32_e32 vcc, v139, v76
	s_nop 1
	v_cndmask_b32_e32 v183, v178, v31, vcc
	v_cmp_lt_u32_e32 vcc, v140, v76
	s_nop 1
	v_cndmask_b32_e32 v32, v178, v32, vcc
	v_cmp_lt_u32_e32 vcc, v141, v76
	s_nop 1
	v_cndmask_b32_e32 v33, v178, v33, vcc
	v_cmp_lt_u32_e32 vcc, v142, v76
	s_nop 1
	v_cndmask_b32_e32 v186, v178, v2, vcc
	v_cmp_lt_u32_e32 vcc, v143, v76
	v_max3_f32 v2, v178, v50, v51
	v_max3_f32 v2, v2, v54, v55
	s_nop 0
	v_cndmask_b32_e32 v187, v178, v3, vcc
	v_max3_f32 v3, v178, v52, v53
	v_cmp_lt_u32_e32 vcc, v144, v76
	v_max3_f32 v3, v3, v56, v57
	v_max3_f32 v2, v2, v58, v59
	v_max3_f32 v3, v3, v60, v61
	v_max3_f32 v2, v2, v62, v63
	s_nop 0
	v_cndmask_b32_e32 v188, v178, v4, vcc
	v_cmp_lt_u32_e32 vcc, v145, v76
	v_max3_f32 v3, v3, v64, v65
	v_max3_f32 v2, v2, v34, v35
	v_max3_f32 v3, v3, v36, v37
	v_max3_f32 v2, v2, v38, v39
	s_nop 0
	v_cndmask_b32_e32 v189, v178, v5, vcc
	v_cmp_lt_u32_e32 vcc, v146, v76
	v_max3_f32 v3, v3, v40, v41
	v_max3_f32 v2, v2, v42, v43
	v_max3_f32 v3, v3, v44, v45
	v_max3_f32 v2, v2, v46, v47
	s_nop 0
	v_cndmask_b32_e32 v190, v178, v6, vcc
	v_cmp_lt_u32_e32 vcc, v147, v76
	v_max3_f32 v3, v3, v48, v49
	v_max3_f32 v2, v2, v87, v89
	v_max3_f32 v3, v3, v91, v92
	v_max3_f32 v2, v2, v93, v94
	s_nop 0
	v_cndmask_b32_e32 v191, v178, v7, vcc
	v_cmp_lt_u32_e32 vcc, v148, v76
	v_max3_f32 v3, v3, v24, v25
	v_max3_f32 v2, v2, v26, v27
	v_max3_f32 v3, v3, v95, v96
	v_max3_f32 v2, v2, v97, v183
	s_nop 0
	v_cndmask_b32_e32 v8, v178, v8, vcc
	v_cmp_lt_u32_e32 vcc, v149, v76
	v_max3_f32 v3, v3, v32, v33
	v_max3_f32 v2, v2, v186, v187
	v_max3_f32 v3, v3, v188, v189
	v_max3_f32 v2, v2, v190, v191
	s_nop 0
	v_cndmask_b32_e32 v9, v178, v9, vcc
	v_cmp_lt_u32_e32 vcc, v150, v76
	v_max3_f32 v3, v3, v8, v9
	s_nop 1
	v_cndmask_b32_e32 v10, v178, v10, vcc
	v_cmp_lt_u32_e32 vcc, v151, v76
	s_nop 1
	v_cndmask_b32_e32 v11, v178, v11, vcc
	v_cmp_lt_u32_e32 vcc, v152, v76
	v_max3_f32 v2, v2, v10, v11
	s_nop 1
	v_cndmask_b32_e32 v196, v178, v12, vcc
	v_cmp_lt_u32_e32 vcc, v153, v76
	s_nop 1
	v_cndmask_b32_e32 v197, v178, v13, vcc
	v_cmp_lt_u32_e32 vcc, v154, v76
	v_max3_f32 v3, v3, v196, v197
	s_nop 1
	v_cndmask_b32_e32 v198, v178, v14, vcc
	v_cmp_lt_u32_e32 vcc, v155, v76
	s_nop 1
	v_cndmask_b32_e32 v199, v178, v15, vcc
	v_cmp_lt_u32_e32 vcc, v156, v76
	v_max3_f32 v2, v2, v198, v199
	s_nop 1
	v_cndmask_b32_e32 v200, v178, v16, vcc
	v_cmp_lt_u32_e32 vcc, v157, v76
	s_nop 1
	v_cndmask_b32_e32 v76, v178, v17, vcc
	v_max3_f32 v3, v3, v200, v76
	v_max3_f32 v2, v2, v3, v3
	v_mov_b32_e32 v3, v2
	s_nop 1
	v_permlane32_swap_b32_e32 v2, v3
	v_max_f32_e32 v3, v3, v3
	v_max_f32_e32 v2, v2, v2
	v_max_f32_e32 v2, v2, v3
	v_cndmask_b32_e64 v201, v2, 0, s[10:11]
	v_sub_f32_e32 v2, v50, v201
	v_exp_f32_e32 v2, v2
	v_sub_f32_e32 v3, v51, v201
	v_exp_f32_e32 v3, v3
	v_sub_f32_e32 v4, v52, v201
	v_exp_f32_e32 v4, v4
	v_sub_f32_e32 v5, v53, v201
	v_exp_f32_e32 v5, v5
	v_add_f32_e32 v6, 0, v2
	v_add_f32_e32 v6, v3, v6
	v_add_f32_e32 v6, v4, v6
	v_add_f32_e32 v14, v5, v6
	v_sub_f32_e32 v6, v54, v201
	v_exp_f32_e32 v6, v6
	v_sub_f32_e32 v7, v55, v201
	v_exp_f32_e32 v7, v7
	v_sub_f32_e32 v12, v56, v201
	v_exp_f32_e32 v12, v12
	v_sub_f32_e32 v13, v57, v201
	v_exp_f32_e32 v13, v13
	v_add_f32_e32 v14, v6, v14
	v_add_f32_e32 v14, v7, v14
	v_add_f32_e32 v14, v12, v14
	v_add_f32_e32 v18, v13, v14
	v_sub_f32_e32 v14, v58, v201
	v_exp_f32_e32 v14, v14
	v_sub_f32_e32 v15, v59, v201
	v_exp_f32_e32 v15, v15
	v_sub_f32_e32 v16, v60, v201
	v_exp_f32_e32 v16, v16
	v_sub_f32_e32 v17, v61, v201
	v_exp_f32_e32 v17, v17
	v_add_f32_e32 v18, v14, v18
	v_add_f32_e32 v18, v15, v18
	v_add_f32_e32 v18, v16, v18
	v_add_f32_e32 v22, v17, v18
	v_sub_f32_e32 v18, v62, v201
	v_exp_f32_e32 v18, v18
	v_sub_f32_e32 v19, v63, v201
	v_exp_f32_e32 v19, v19
	v_sub_f32_e32 v20, v64, v201
	v_exp_f32_e32 v20, v20
	v_sub_f32_e32 v21, v65, v201
	v_exp_f32_e32 v21, v21
	v_add_f32_e32 v22, v18, v22
	v_add_f32_e32 v22, v19, v22
	v_add_f32_e32 v22, v20, v22
	v_add_f32_e32 v30, v21, v22
	v_sub_f32_e32 v22, v34, v201
	v_exp_f32_e32 v22, v22
	v_sub_f32_e32 v23, v35, v201
	v_exp_f32_e32 v23, v23
	v_sub_f32_e32 v28, v36, v201
	v_exp_f32_e32 v28, v28
	v_sub_f32_e32 v29, v37, v201
	v_exp_f32_e32 v29, v29
	v_add_f32_e32 v30, v22, v30
	v_add_f32_e32 v30, v23, v30
	v_add_f32_e32 v30, v28, v30
	v_add_f32_e32 v36, v29, v30
	v_sub_f32_e32 v30, v38, v201
	v_exp_f32_e32 v30, v30
	v_sub_f32_e32 v31, v39, v201
	v_exp_f32_e32 v31, v31
	v_sub_f32_e32 v34, v40, v201
	v_exp_f32_e32 v34, v34
	v_sub_f32_e32 v35, v41, v201
	v_exp_f32_e32 v35, v35
	v_add_f32_e32 v36, v30, v36
	v_add_f32_e32 v36, v31, v36
	v_add_f32_e32 v36, v34, v36
	v_add_f32_e32 v40, v35, v36
	v_sub_f32_e32 v36, v42, v201
	v_exp_f32_e32 v36, v36
	v_sub_f32_e32 v37, v43, v201
	v_exp_f32_e32 v37, v37
	v_sub_f32_e32 v38, v44, v201
	v_exp_f32_e32 v38, v38
	v_sub_f32_e32 v39, v45, v201
	v_exp_f32_e32 v39, v39
	v_add_f32_e32 v40, v36, v40
	v_add_f32_e32 v40, v37, v40
	v_add_f32_e32 v40, v38, v40
	v_add_f32_e32 v44, v39, v40
	v_sub_f32_e32 v40, v46, v201
	v_exp_f32_e32 v40, v40
	v_sub_f32_e32 v41, v47, v201
	v_exp_f32_e32 v41, v41
	v_sub_f32_e32 v42, v48, v201
	v_exp_f32_e32 v42, v42
	v_sub_f32_e32 v43, v49, v201
	v_exp_f32_e32 v43, v43
	v_add_f32_e32 v44, v40, v44
	v_add_f32_e32 v44, v41, v44
	v_add_f32_e32 v44, v42, v44
	v_add_f32_e32 v48, v43, v44
	v_sub_f32_e32 v44, v87, v201
	v_exp_f32_e32 v44, v44
	v_sub_f32_e32 v45, v89, v201
	v_exp_f32_e32 v45, v45
	v_sub_f32_e32 v46, v91, v201
	v_exp_f32_e32 v46, v46
	v_sub_f32_e32 v47, v92, v201
	v_exp_f32_e32 v47, v47
	v_add_f32_e32 v48, v44, v48
	v_add_f32_e32 v48, v45, v48
	v_add_f32_e32 v48, v46, v48
	v_add_f32_e32 v52, v47, v48
	v_sub_f32_e32 v48, v93, v201
	v_exp_f32_e32 v48, v48
	v_sub_f32_e32 v49, v94, v201
	v_exp_f32_e32 v49, v49
	v_sub_f32_e32 v24, v24, v201
	v_exp_f32_e32 v50, v24
	v_sub_f32_e32 v24, v25, v201
	v_exp_f32_e32 v51, v24
	v_sub_f32_e32 v25, v26, v201
	v_add_f32_e32 v24, v48, v52
	v_exp_f32_e32 v52, v25
	v_sub_f32_e32 v25, v27, v201
	v_add_f32_e32 v24, v49, v24
	v_exp_f32_e32 v53, v25
	v_sub_f32_e32 v25, v95, v201
	v_add_f32_e32 v24, v50, v24
	v_exp_f32_e32 v54, v25
	v_sub_f32_e32 v25, v96, v201
	v_add_f32_e32 v24, v51, v24
	v_exp_f32_e32 v55, v25
	v_sub_f32_e32 v25, v97, v201
	v_add_f32_e32 v24, v52, v24
	v_exp_f32_e32 v182, v25
	v_sub_f32_e32 v25, v183, v201
	v_add_f32_e32 v24, v53, v24
	v_exp_f32_e32 v183, v25
	v_sub_f32_e32 v25, v32, v201
	v_add_f32_e32 v24, v54, v24
	v_exp_f32_e32 v184, v25
	v_sub_f32_e32 v25, v33, v201
	v_add_f32_e32 v24, v55, v24
	v_exp_f32_e32 v185, v25
	v_sub_f32_e32 v25, v186, v201
	v_add_f32_e32 v24, v182, v24
	v_exp_f32_e32 v186, v25
	v_sub_f32_e32 v25, v187, v201
	v_add_f32_e32 v24, v183, v24
	v_exp_f32_e32 v187, v25
	v_sub_f32_e32 v25, v188, v201
	v_add_f32_e32 v24, v184, v24
	v_exp_f32_e32 v188, v25
	v_sub_f32_e32 v25, v189, v201
	v_add_f32_e32 v24, v185, v24
	v_exp_f32_e32 v189, v25
	v_sub_f32_e32 v25, v190, v201
	v_add_f32_e32 v24, v186, v24
	v_exp_f32_e32 v190, v25
	v_sub_f32_e32 v25, v191, v201
	v_add_f32_e32 v24, v187, v24
	v_exp_f32_e32 v191, v25
	v_sub_f32_e32 v8, v8, v201
	v_add_f32_e32 v24, v188, v24
	v_exp_f32_e32 v192, v8
	v_sub_f32_e32 v8, v9, v201
	v_add_f32_e32 v24, v189, v24
	v_exp_f32_e32 v193, v8
	v_sub_f32_e32 v9, v10, v201
	v_add_f32_e32 v8, v190, v24
	v_exp_f32_e32 v194, v9
	v_sub_f32_e32 v9, v11, v201
	v_add_f32_e32 v8, v191, v8
	v_exp_f32_e32 v195, v9
	v_sub_f32_e32 v9, v196, v201
	v_add_f32_e32 v8, v192, v8
	v_exp_f32_e32 v196, v9
	v_sub_f32_e32 v9, v197, v201
	v_add_f32_e32 v8, v193, v8
	v_exp_f32_e32 v197, v9
	v_sub_f32_e32 v9, v198, v201
	v_add_f32_e32 v8, v194, v8
	v_exp_f32_e32 v198, v9
	v_sub_f32_e32 v9, v199, v201
	v_add_f32_e32 v8, v195, v8
	v_exp_f32_e32 v199, v9
	v_sub_f32_e32 v9, v200, v201
	v_add_f32_e32 v8, v196, v8
	v_exp_f32_e32 v200, v9
	v_sub_f32_e32 v9, v76, v201
	v_add_f32_e32 v8, v197, v8
	v_exp_f32_e32 v201, v9
	v_add_f32_e32 v8, v198, v8
	v_add_f32_e32 v8, v199, v8
	v_add_f32_e32 v8, v200, v8
	v_add_f32_e32 v8, v201, v8
	v_mov_b32_e32 v9, v8
	s_nop 1
	v_permlane32_swap_b32_e32 v8, v9
	v_add_f32_e32 v8, v8, v9
	v_div_scale_f32 v9, s[40:41], v8, v8, 1.0
	v_rcp_f32_e32 v10, v9
	s_add_i32 s40, s31, 0
	s_add_i32 s40, s40, 0x10a00
	v_fma_f32 v11, -v9, v10, 1.0
	v_fmac_f32_e32 v10, v11, v10
	v_div_scale_f32 v11, vcc, 1.0, v8, 1.0
	v_mul_f32_e32 v24, v11, v10
	v_fma_f32 v25, -v9, v24, v11
	v_fmac_f32_e32 v24, v25, v10
	v_fma_f32 v9, -v9, v24, v11
	v_div_fmas_f32 v9, v9, v10, v24
	v_div_fixup_f32 v8, v9, v8, 1.0
	v_cndmask_b32_e64 v76, v8, 0, s[10:11]
	v_pk_mul_f32 v[10:11], v[76:77], v[2:3] op_sel_hi:[0,1]
	v_pk_mul_f32 v[8:9], v[76:77], v[4:5] op_sel_hi:[0,1]
	v_pk_mul_f32 v[6:7], v[76:77], v[6:7] op_sel_hi:[0,1]
	v_pk_mul_f32 v[4:5], v[76:77], v[12:13] op_sel_hi:[0,1]
	v_add_f32_e32 v12, v8, v9
	v_add_f32_e32 v13, v10, v11
	v_pk_mul_f32 v[2:3], v[76:77], v[14:15] op_sel_hi:[0,1]
	v_pk_mul_f32 v[24:25], v[76:77], v[16:17] op_sel_hi:[0,1]
	v_add_f32_e32 v12, v13, v12
	v_add_f32_e32 v13, v4, v5
	v_add_f32_e32 v14, v6, v7
	v_pk_mul_f32 v[26:27], v[76:77], v[18:19] op_sel_hi:[0,1]
	v_pk_mul_f32 v[32:33], v[76:77], v[20:21] op_sel_hi:[0,1]
	v_add_f32_e32 v13, v14, v13
	v_add_f32_e32 v14, v24, v25
	v_add_f32_e32 v15, v2, v3
	v_pk_mul_f32 v[92:93], v[76:77], v[22:23] op_sel_hi:[0,1]
	v_pk_mul_f32 v[94:95], v[76:77], v[28:29] op_sel_hi:[0,1]
	v_add_f32_e32 v14, v15, v14
	v_add_f32_e32 v15, v32, v33
	v_add_f32_e32 v16, v26, v27
	v_pk_mul_f32 v[96:97], v[76:77], v[30:31] op_sel_hi:[0,1]
	v_pk_mul_f32 v[28:29], v[76:77], v[34:35] op_sel_hi:[0,1]
	v_add_f32_e32 v15, v16, v15
	v_add_f32_e32 v16, v94, v95
	v_add_f32_e32 v17, v92, v93
	v_pk_mul_f32 v[30:31], v[76:77], v[36:37] op_sel_hi:[0,1]
	v_pk_mul_f32 v[18:19], v[76:77], v[38:39] op_sel_hi:[0,1]
	v_pk_mul_f32 v[20:21], v[76:77], v[40:41] op_sel_hi:[0,1]
	v_pk_mul_f32 v[22:23], v[76:77], v[42:43] op_sel_hi:[0,1]
	v_pk_mul_f32 v[64:65], v[76:77], v[44:45] op_sel_hi:[0,1]
	v_pk_mul_f32 v[62:63], v[76:77], v[46:47] op_sel_hi:[0,1]
	v_pk_mul_f32 v[60:61], v[76:77], v[48:49] op_sel_hi:[0,1]
	v_pk_mul_f32 v[58:59], v[76:77], v[50:51] op_sel_hi:[0,1]
	v_pk_mul_f32 v[56:57], v[76:77], v[52:53] op_sel_hi:[0,1]
	v_pk_mul_f32 v[40:41], v[76:77], v[54:55] op_sel_hi:[0,1]
	v_pk_mul_f32 v[42:43], v[76:77], v[182:183] op_sel_hi:[0,1]
	v_pk_mul_f32 v[48:49], v[76:77], v[184:185] op_sel_hi:[0,1]
	v_pk_mul_f32 v[50:51], v[76:77], v[186:187] op_sel_hi:[0,1]
	v_pk_mul_f32 v[52:53], v[76:77], v[188:189] op_sel_hi:[0,1]
	v_pk_mul_f32 v[54:55], v[76:77], v[190:191] op_sel_hi:[0,1]
	v_pk_mul_f32 v[44:45], v[76:77], v[192:193] op_sel_hi:[0,1]
	v_pk_mul_f32 v[46:47], v[76:77], v[194:195] op_sel_hi:[0,1]
	v_pk_mul_f32 v[34:35], v[76:77], v[196:197] op_sel_hi:[0,1]
	v_pk_mul_f32 v[36:37], v[76:77], v[198:199] op_sel_hi:[0,1]
	v_pk_mul_f32 v[38:39], v[76:77], v[200:201] op_sel_hi:[0,1]
	v_add_f32_e32 v16, v17, v16
	v_add_f32_e32 v17, v28, v29
	v_add_f32_e32 v76, v96, v97
	v_add_f32_e32 v17, v76, v17
	v_add_f32_e32 v76, v18, v19
	v_add_f32_e32 v87, v30, v31
	v_add_f32_e32 v76, v87, v76
	v_add_f32_e32 v87, v22, v23
	v_add_f32_e32 v89, v20, v21
	v_add_f32_e32 v87, v89, v87
	v_add_f32_e32 v89, v62, v63
	v_add_f32_e32 v91, v64, v65
	v_add_f32_e32 v89, v91, v89
	v_add_f32_e32 v91, v58, v59
	v_add_f32_e32 v182, v60, v61
	v_add_f32_e32 v91, v182, v91
	v_add_f32_e32 v182, v40, v41
	v_add_f32_e32 v183, v56, v57
	v_add_f32_e32 v182, v183, v182
	v_add_f32_e32 v183, v48, v49
	v_add_f32_e32 v184, v42, v43
	v_add_f32_e32 v183, v184, v183
	v_add_f32_e32 v184, v52, v53
	v_add_f32_e32 v185, v50, v51
	v_add_f32_e32 v184, v185, v184
	v_add_f32_e32 v185, v44, v45
	v_add_f32_e32 v186, v54, v55
	v_add_f32_e32 v185, v186, v185
	v_add_f32_e32 v186, v34, v35
	v_add_f32_e32 v187, v46, v47
	v_add_f32_e32 v186, v187, v186
	v_add_f32_e32 v187, v38, v39
	v_add_f32_e32 v188, v36, v37
	v_add_f32_e32 v187, v188, v187
	v_mov_b32_e32 v188, v9
	v_mov_b32_e32 v189, v9
	s_nop 1
	v_permlane32_swap_b32_e32 v188, v189
	v_cndmask_b32_e64 v188, v188, v189, s[2:3]
	v_cndmask_b32_e64 v189, v188, 0, s[4:5]
	v_add_f32_e32 v12, v189, v12
	v_mov_b32_e32 v189, v5
	v_mov_b32_e32 v190, v5
	s_nop 1
	v_permlane32_swap_b32_e32 v189, v190
	v_cndmask_b32_e64 v189, v189, v190, s[2:3]
	v_cndmask_b32_e64 v188, v189, v188, s[4:5]
	v_add_f32_e32 v188, v188, v13
	v_mov_b32_e32 v13, v25
	v_mov_b32_e32 v190, v25
	s_nop 1
	v_permlane32_swap_b32_e32 v13, v190
	v_cndmask_b32_e64 v13, v13, v190, s[2:3]
	v_cndmask_b32_e64 v189, v13, v189, s[4:5]
	v_add_f32_e32 v189, v189, v14
	v_mov_b32_e32 v14, v33
	v_mov_b32_e32 v190, v33
	s_nop 1
	v_permlane32_swap_b32_e32 v14, v190
	v_cndmask_b32_e64 v14, v14, v190, s[2:3]
	v_cndmask_b32_e64 v13, v14, v13, s[4:5]
	v_add_f32_e32 v190, v15, v13
	v_mov_b32_e32 v13, v95
	v_mov_b32_e32 v15, v95
	s_nop 1
	v_permlane32_swap_b32_e32 v13, v15
	v_cndmask_b32_e64 v13, v13, v15, s[2:3]
	v_cndmask_b32_e64 v14, v13, v14, s[4:5]
	v_add_f32_e32 v191, v16, v14
	v_mov_b32_e32 v14, v29
	v_mov_b32_e32 v15, v29
	s_nop 1
	v_permlane32_swap_b32_e32 v14, v15
	v_cndmask_b32_e64 v14, v14, v15, s[2:3]
	v_cndmask_b32_e64 v13, v14, v13, s[4:5]
	v_add_f32_e32 v192, v17, v13
	v_mov_b32_e32 v13, v19
	v_mov_b32_e32 v15, v19
	s_nop 1
	v_permlane32_swap_b32_e32 v13, v15
	v_cndmask_b32_e64 v13, v13, v15, s[2:3]
	v_cndmask_b32_e64 v14, v13, v14, s[4:5]
	v_add_f32_e32 v193, v76, v14
	v_mov_b32_e32 v14, v23
	v_mov_b32_e32 v15, v23
	s_nop 1
	v_permlane32_swap_b32_e32 v14, v15
	v_cndmask_b32_e64 v14, v14, v15, s[2:3]
	v_cndmask_b32_e64 v13, v14, v13, s[4:5]
	v_add_f32_e32 v194, v87, v13
	v_mov_b32_e32 v13, v63
	v_mov_b32_e32 v15, v63
	s_nop 1
	v_permlane32_swap_b32_e32 v13, v15
	v_cndmask_b32_e64 v13, v13, v15, s[2:3]
	v_cndmask_b32_e64 v14, v13, v14, s[4:5]
	v_add_f32_e32 v195, v89, v14
	v_mov_b32_e32 v14, v59
	v_mov_b32_e32 v15, v59
	s_nop 1
	v_permlane32_swap_b32_e32 v14, v15
	v_cndmask_b32_e64 v14, v14, v15, s[2:3]
	v_cndmask_b32_e64 v13, v14, v13, s[4:5]
	v_add_f32_e32 v196, v91, v13
	v_mov_b32_e32 v13, v41
	v_mov_b32_e32 v15, v41
	s_nop 1
	v_permlane32_swap_b32_e32 v13, v15
	v_cndmask_b32_e64 v13, v13, v15, s[2:3]
	v_cndmask_b32_e64 v14, v13, v14, s[4:5]
	v_add_f32_e32 v197, v182, v14
	v_mov_b32_e32 v14, v49
	v_mov_b32_e32 v15, v49
	s_nop 1
	v_permlane32_swap_b32_e32 v14, v15
	v_cndmask_b32_e64 v14, v14, v15, s[2:3]
	v_cndmask_b32_e64 v13, v14, v13, s[4:5]
	v_add_f32_e32 v198, v183, v13
	v_mov_b32_e32 v13, v53
	v_mov_b32_e32 v15, v53
	s_nop 1
	v_permlane32_swap_b32_e32 v13, v15
	v_cndmask_b32_e64 v13, v13, v15, s[2:3]
	v_cndmask_b32_e64 v14, v13, v14, s[4:5]
	v_add_f32_e32 v199, v184, v14
	v_mov_b32_e32 v14, v45
	v_mov_b32_e32 v15, v45
	s_nop 1
	v_permlane32_swap_b32_e32 v14, v15
	v_cndmask_b32_e64 v14, v14, v15, s[2:3]
	v_cndmask_b32_e64 v13, v14, v13, s[4:5]
	v_add_f32_e32 v200, v185, v13
	v_mov_b32_e32 v13, v35
	v_mov_b32_e32 v15, v35
	s_nop 1
	v_permlane32_swap_b32_e32 v13, v15
	v_cndmask_b32_e64 v13, v13, v15, s[2:3]
	v_cndmask_b32_e64 v14, v13, v14, s[4:5]
	v_add_f32_e32 v201, v186, v14
	v_mov_b32_e32 v14, v39
	v_mov_b32_e32 v15, v39
	s_nop 1
	v_permlane32_swap_b32_e32 v14, v15
	v_cndmask_b32_e64 v14, v14, v15, s[2:3]
	v_cndmask_b32_e64 v13, v14, v13, s[4:5]
	v_add_f32_e32 v202, v187, v13
	v_add_f32_dpp v12, v12, v12 quad_perm:[1,0,3,2] row_mask:0xf bank_mask:0xf bound_ctrl:1
	v_mov_b32_e32 v13, v77
	v_add_f32_dpp v14, v188, v188 quad_perm:[1,0,3,2] row_mask:0xf bank_mask:0xf bound_ctrl:1
	v_mov_b32_e32 v15, v77
	v_add_f32_dpp v16, v189, v189 quad_perm:[1,0,3,2] row_mask:0xf bank_mask:0xf bound_ctrl:1
	v_mov_b32_e32 v17, v77
	v_add_f32_dpp v76, v190, v190 quad_perm:[1,0,3,2] row_mask:0xf bank_mask:0xf bound_ctrl:1
	v_mov_b32_e32 v87, v77
	v_add_f32_dpp v89, v191, v191 quad_perm:[1,0,3,2] row_mask:0xf bank_mask:0xf bound_ctrl:1
	v_mov_b32_e32 v91, v77
	v_add_f32_dpp v182, v192, v192 quad_perm:[1,0,3,2] row_mask:0xf bank_mask:0xf bound_ctrl:1
	v_mov_b32_e32 v183, v77
	v_add_f32_dpp v184, v193, v193 quad_perm:[1,0,3,2] row_mask:0xf bank_mask:0xf bound_ctrl:1
	v_mov_b32_e32 v185, v77
	v_add_f32_dpp v186, v194, v194 quad_perm:[1,0,3,2] row_mask:0xf bank_mask:0xf bound_ctrl:1
	v_mov_b32_e32 v187, v77
	v_add_f32_dpp v188, v195, v195 quad_perm:[1,0,3,2] row_mask:0xf bank_mask:0xf bound_ctrl:1
	v_mov_b32_e32 v189, v77
	v_add_f32_dpp v190, v196, v196 quad_perm:[1,0,3,2] row_mask:0xf bank_mask:0xf bound_ctrl:1
	v_mov_b32_e32 v191, v77
	v_add_f32_dpp v192, v197, v197 quad_perm:[1,0,3,2] row_mask:0xf bank_mask:0xf bound_ctrl:1
	v_mov_b32_e32 v193, v77
	v_add_f32_dpp v194, v198, v198 quad_perm:[1,0,3,2] row_mask:0xf bank_mask:0xf bound_ctrl:1
	v_mov_b32_e32 v195, v77
	v_add_f32_dpp v196, v199, v199 quad_perm:[1,0,3,2] row_mask:0xf bank_mask:0xf bound_ctrl:1
	v_mov_b32_e32 v197, v77
	v_add_f32_dpp v198, v200, v200 quad_perm:[1,0,3,2] row_mask:0xf bank_mask:0xf bound_ctrl:1
	v_mov_b32_e32 v199, v77
	v_add_f32_dpp v200, v201, v201 quad_perm:[1,0,3,2] row_mask:0xf bank_mask:0xf bound_ctrl:1
	v_mov_b32_e32 v201, v77
	v_add_f32_dpp v202, v202, v202 quad_perm:[1,0,3,2] row_mask:0xf bank_mask:0xf bound_ctrl:1
	v_mov_b32_dpp v13, v12 quad_perm:[2,3,0,1] row_mask:0xf bank_mask:0xf
	v_mov_b32_dpp v15, v14 quad_perm:[2,3,0,1] row_mask:0xf bank_mask:0xf
	v_mov_b32_dpp v17, v16 quad_perm:[2,3,0,1] row_mask:0xf bank_mask:0xf
	v_mov_b32_dpp v87, v76 quad_perm:[2,3,0,1] row_mask:0xf bank_mask:0xf
	v_mov_b32_dpp v91, v89 quad_perm:[2,3,0,1] row_mask:0xf bank_mask:0xf
	v_mov_b32_dpp v183, v182 quad_perm:[2,3,0,1] row_mask:0xf bank_mask:0xf
	v_mov_b32_dpp v185, v184 quad_perm:[2,3,0,1] row_mask:0xf bank_mask:0xf
	v_mov_b32_dpp v187, v186 quad_perm:[2,3,0,1] row_mask:0xf bank_mask:0xf
	v_mov_b32_dpp v189, v188 quad_perm:[2,3,0,1] row_mask:0xf bank_mask:0xf
	v_mov_b32_dpp v191, v190 quad_perm:[2,3,0,1] row_mask:0xf bank_mask:0xf
	v_mov_b32_dpp v193, v192 quad_perm:[2,3,0,1] row_mask:0xf bank_mask:0xf
	v_mov_b32_dpp v195, v194 quad_perm:[2,3,0,1] row_mask:0xf bank_mask:0xf
	v_mov_b32_dpp v197, v196 quad_perm:[2,3,0,1] row_mask:0xf bank_mask:0xf
	v_mov_b32_dpp v199, v198 quad_perm:[2,3,0,1] row_mask:0xf bank_mask:0xf
	v_mov_b32_dpp v201, v200 quad_perm:[2,3,0,1] row_mask:0xf bank_mask:0xf
	v_mov_b32_dpp v203, v202 quad_perm:[2,3,0,1] row_mask:0xf bank_mask:0xf
	s_and_saveexec_b64 s[10:11], s[6:7]
	s_cbranch_execz .LBB0_556
	v_add_f32_e32 v12, v12, v13
	v_lshlrev_b32_e32 v13, 2, v74
	v_add_f32_e32 v14, v14, v15
	v_add3_u32 v13, s40, v158, v13
	v_add_f32_e32 v202, v202, v203
	v_add_f32_e32 v200, v200, v201
	v_add_f32_e32 v198, v198, v199
	v_add_f32_e32 v196, v196, v197
	v_add_f32_e32 v194, v194, v195
	v_add_f32_e32 v192, v192, v193
	v_add_f32_e32 v190, v190, v191
	v_add_f32_e32 v188, v188, v189
	v_add_f32_e32 v186, v186, v187
	v_add_f32_e32 v184, v184, v185
	v_add_f32_e32 v182, v182, v183
	v_add_f32_e32 v89, v89, v91
	v_add_f32_e32 v76, v76, v87
	v_add_f32_e32 v16, v16, v17
	ds_write2_b32 v13, v12, v14 offset1:2
	ds_write2_b32 v13, v16, v76 offset0:4 offset1:6
	ds_write2_b32 v13, v89, v182 offset0:8 offset1:10
	ds_write2_b32 v13, v184, v186 offset0:12 offset1:14
	ds_write2_b32 v13, v188, v190 offset0:16 offset1:18
	ds_write2_b32 v13, v192, v194 offset0:20 offset1:22
	ds_write2_b32 v13, v196, v198 offset0:24 offset1:26
	ds_write2_b32 v13, v200, v202 offset0:28 offset1:30

.LBB0_652:
	s_nop 0
	v_max3_f32 v170, v114, v98, v115
	v_max3_f32 v190, v99, v116, v100
	v_max3_f32 v191, v129, v113, v129
	v_max3_f32 v170, v170, v117, v101
	v_max3_f32 v190, v190, v118, v102
	v_max3_f32 v170, v170, v119, v103
	v_max3_f32 v190, v190, v120, v104
	v_max3_f32 v170, v170, v121, v105
	v_max3_f32 v190, v190, v122, v106
	v_max3_f32 v170, v170, v123, v107
	v_max3_f32 v190, v190, v124, v108
	v_max3_f32 v170, v170, v125, v109
	v_max3_f32 v190, v190, v126, v110
	v_max3_f32 v170, v170, v127, v111
	v_max3_f32 v190, v190, v128, v112
	v_max3_f32 v170, v170, v190, v191
	v_mov_b32_e32 v190, v170
	s_nop 1
	v_permlane32_swap_b32_e32 v170, v190
	v_max3_f32 v170, v170, v190, v190
	v_cmp_lt_f32_e32 vcc, s39, v170
	s_cbranch_vccz .LBB0_656
	v_max3_f32 v170, v170, v163, v163
	v_exp_f32_e64 v190, -v170
	s_and_saveexec_b64 s[12:13], s[2:3]
	ds_write_b32 v174, v190
	s_or_b64 exec, exec, s[12:13]
	s_waitcnt lgkmcnt(0)
	ds_read_b128 v[192:195], v165 offset:64
	ds_read_b128 v[196:199], v165 offset:96
	ds_read_b128 v[200:203], v165
	ds_read_b128 v[204:207], v165 offset:32
	s_waitcnt lgkmcnt(0)
	v_add_f32_e32 v189, v189, v170
	v_pk_add_f32 v[114:115], v[114:115], v[170:171] op_sel_hi:[1,0] neg_lo:[0,1] neg_hi:[0,1]
	v_pk_add_f32 v[98:99], v[98:99], v[170:171] op_sel_hi:[1,0] neg_lo:[0,1] neg_hi:[0,1]
	v_pk_add_f32 v[116:117], v[116:117], v[170:171] op_sel_hi:[1,0] neg_lo:[0,1] neg_hi:[0,1]
	v_pk_add_f32 v[100:101], v[100:101], v[170:171] op_sel_hi:[1,0] neg_lo:[0,1] neg_hi:[0,1]
	v_pk_add_f32 v[118:119], v[118:119], v[170:171] op_sel_hi:[1,0] neg_lo:[0,1] neg_hi:[0,1]
	v_pk_add_f32 v[102:103], v[102:103], v[170:171] op_sel_hi:[1,0] neg_lo:[0,1] neg_hi:[0,1]
	v_pk_add_f32 v[120:121], v[120:121], v[170:171] op_sel_hi:[1,0] neg_lo:[0,1] neg_hi:[0,1]
	v_pk_add_f32 v[104:105], v[104:105], v[170:171] op_sel_hi:[1,0] neg_lo:[0,1] neg_hi:[0,1]
	v_pk_add_f32 v[122:123], v[122:123], v[170:171] op_sel_hi:[1,0] neg_lo:[0,1] neg_hi:[0,1]
	v_pk_add_f32 v[106:107], v[106:107], v[170:171] op_sel_hi:[1,0] neg_lo:[0,1] neg_hi:[0,1]
	v_pk_add_f32 v[124:125], v[124:125], v[170:171] op_sel_hi:[1,0] neg_lo:[0,1] neg_hi:[0,1]
	v_pk_add_f32 v[108:109], v[108:109], v[170:171] op_sel_hi:[1,0] neg_lo:[0,1] neg_hi:[0,1]
	v_pk_add_f32 v[126:127], v[126:127], v[170:171] op_sel_hi:[1,0] neg_lo:[0,1] neg_hi:[0,1]
	v_pk_add_f32 v[110:111], v[110:111], v[170:171] op_sel_hi:[1,0] neg_lo:[0,1] neg_hi:[0,1]
	v_pk_add_f32 v[128:129], v[128:129], v[170:171] op_sel_hi:[1,0] neg_lo:[0,1] neg_hi:[0,1]
	v_pk_add_f32 v[112:113], v[112:113], v[170:171] op_sel_hi:[1,0] neg_lo:[0,1] neg_hi:[0,1]
	v_mul_f32_e32 v181, v181, v190
	s_waitcnt lgkmcnt(0)
	v_pk_mul_f32 v[64:65], v[64:65], v[198:199]
	v_pk_mul_f32 v[60:61], v[60:61], v[194:195]
	v_pk_mul_f32 v[56:57], v[56:57], v[206:207]
	v_pk_mul_f32 v[52:53], v[52:53], v[202:203]
	v_pk_mul_f32 v[62:63], v[62:63], v[196:197]
	v_pk_mul_f32 v[58:59], v[58:59], v[192:193]
	v_pk_mul_f32 v[54:55], v[54:55], v[204:205]
	v_pk_mul_f32 v[50:51], v[50:51], v[200:201]
	v_pk_mul_f32 v[48:49], v[48:49], v[198:199]
	v_pk_mul_f32 v[44:45], v[44:45], v[194:195]
	v_pk_mul_f32 v[40:41], v[40:41], v[206:207]
	v_pk_mul_f32 v[36:37], v[36:37], v[202:203]
	v_pk_mul_f32 v[46:47], v[46:47], v[196:197]
	v_pk_mul_f32 v[42:43], v[42:43], v[192:193]
	v_pk_mul_f32 v[38:39], v[38:39], v[204:205]
	v_pk_mul_f32 v[34:35], v[34:35], v[200:201]

.LBB0_660:
	s_nop 0
	v_max3_f32 v170, v82, v66, v83
	v_max3_f32 v190, v67, v84, v68
	v_max3_f32 v191, v97, v81, v97
	v_max3_f32 v170, v170, v85, v69
	v_max3_f32 v190, v190, v86, v70
	v_max3_f32 v170, v170, v87, v71
	v_max3_f32 v190, v190, v88, v72
	v_max3_f32 v170, v170, v89, v73
	v_max3_f32 v190, v190, v90, v74
	v_max3_f32 v170, v170, v91, v75
	v_max3_f32 v190, v190, v92, v76
	v_max3_f32 v170, v170, v93, v77
	v_max3_f32 v190, v190, v94, v78
	v_max3_f32 v170, v170, v95, v79
	v_max3_f32 v190, v190, v96, v80
	v_max3_f32 v170, v170, v190, v191
	v_mov_b32_e32 v190, v170
	s_nop 1
	v_permlane32_swap_b32_e32 v170, v190
	v_max3_f32 v170, v170, v190, v190
	v_cmp_lt_f32_e32 vcc, s39, v170
	s_cbranch_vccz .LBB0_644
	v_max3_f32 v170, v170, v163, v163
	v_exp_f32_e64 v190, -v170
	s_and_saveexec_b64 s[12:13], s[2:3]
	s_cbranch_execz .LBB0_643
	ds_write_b32 v174, v190
	s_branch .LBB0_643

.LBB0_669:
	s_nop 0
	v_max3_f32 v130, v114, v98, v115
	v_max3_f32 v131, v99, v116, v100
	v_max3_f32 v132, v129, v113, v129
	v_max3_f32 v130, v130, v117, v101
	v_max3_f32 v131, v131, v118, v102
	v_max3_f32 v130, v130, v119, v103
	v_max3_f32 v131, v131, v120, v104
	v_max3_f32 v130, v130, v121, v105
	v_max3_f32 v131, v131, v122, v106
	v_max3_f32 v130, v130, v123, v107
	v_max3_f32 v131, v131, v124, v108
	v_max3_f32 v130, v130, v125, v109
	v_max3_f32 v131, v131, v126, v110
	v_max3_f32 v130, v130, v127, v111
	v_max3_f32 v131, v131, v128, v112
	v_max3_f32 v130, v130, v131, v132
	v_mov_b32_e32 v131, v130
	s_nop 1
	v_permlane32_swap_b32_e32 v130, v131
	v_max3_f32 v130, v130, v131, v131
	v_cmp_lt_f32_e32 vcc, s39, v130
	s_cbranch_vccz .LBB0_673
	v_max3_f32 v130, v130, v163, v163
	v_exp_f32_e64 v131, -v130
	s_and_saveexec_b64 s[10:11], s[2:3]
	ds_write_b32 v174, v131
	s_or_b64 exec, exec, s[10:11]
	s_waitcnt lgkmcnt(0)
	ds_read_b128 v[136:139], v165 offset:64
	ds_read_b128 v[140:143], v165 offset:96
	ds_read_b128 v[144:147], v165
	ds_read_b128 v[148:151], v165 offset:32
	s_waitcnt lgkmcnt(0)
	v_pk_add_f32 v[114:115], v[114:115], v[130:131] op_sel_hi:[1,0] neg_lo:[0,1] neg_hi:[0,1]
	v_pk_add_f32 v[98:99], v[98:99], v[130:131] op_sel_hi:[1,0] neg_lo:[0,1] neg_hi:[0,1]
	v_pk_add_f32 v[116:117], v[116:117], v[130:131] op_sel_hi:[1,0] neg_lo:[0,1] neg_hi:[0,1]
	v_pk_add_f32 v[100:101], v[100:101], v[130:131] op_sel_hi:[1,0] neg_lo:[0,1] neg_hi:[0,1]
	v_pk_add_f32 v[118:119], v[118:119], v[130:131] op_sel_hi:[1,0] neg_lo:[0,1] neg_hi:[0,1]
	v_pk_add_f32 v[102:103], v[102:103], v[130:131] op_sel_hi:[1,0] neg_lo:[0,1] neg_hi:[0,1]
	v_pk_add_f32 v[120:121], v[120:121], v[130:131] op_sel_hi:[1,0] neg_lo:[0,1] neg_hi:[0,1]
	v_pk_add_f32 v[104:105], v[104:105], v[130:131] op_sel_hi:[1,0] neg_lo:[0,1] neg_hi:[0,1]
	v_pk_add_f32 v[122:123], v[122:123], v[130:131] op_sel_hi:[1,0] neg_lo:[0,1] neg_hi:[0,1]
	v_pk_add_f32 v[106:107], v[106:107], v[130:131] op_sel_hi:[1,0] neg_lo:[0,1] neg_hi:[0,1]
	v_pk_add_f32 v[124:125], v[124:125], v[130:131] op_sel_hi:[1,0] neg_lo:[0,1] neg_hi:[0,1]
	v_pk_add_f32 v[108:109], v[108:109], v[130:131] op_sel_hi:[1,0] neg_lo:[0,1] neg_hi:[0,1]
	v_pk_add_f32 v[126:127], v[126:127], v[130:131] op_sel_hi:[1,0] neg_lo:[0,1] neg_hi:[0,1]
	v_pk_add_f32 v[110:111], v[110:111], v[130:131] op_sel_hi:[1,0] neg_lo:[0,1] neg_hi:[0,1]
	v_pk_add_f32 v[128:129], v[128:129], v[130:131] op_sel_hi:[1,0] neg_lo:[0,1] neg_hi:[0,1]
	v_pk_add_f32 v[112:113], v[112:113], v[130:131] op_sel_hi:[1,0] neg_lo:[0,1] neg_hi:[0,1]
	v_mul_f32_e32 v181, v181, v131
	s_waitcnt lgkmcnt(2)
	v_pk_mul_f32 v[64:65], v[64:65], v[142:143]
	v_pk_mul_f32 v[60:61], v[60:61], v[138:139]
	s_waitcnt lgkmcnt(0)
	v_pk_mul_f32 v[56:57], v[56:57], v[150:151]
	v_pk_mul_f32 v[52:53], v[52:53], v[146:147]
	v_pk_mul_f32 v[62:63], v[62:63], v[140:141]
	v_pk_mul_f32 v[58:59], v[58:59], v[136:137]
	v_pk_mul_f32 v[54:55], v[54:55], v[148:149]
	v_pk_mul_f32 v[50:51], v[50:51], v[144:145]
	v_pk_mul_f32 v[48:49], v[48:49], v[142:143]
	v_pk_mul_f32 v[44:45], v[44:45], v[138:139]
	v_pk_mul_f32 v[40:41], v[40:41], v[150:151]
	v_pk_mul_f32 v[36:37], v[36:37], v[146:147]
	v_pk_mul_f32 v[46:47], v[46:47], v[140:141]
	v_pk_mul_f32 v[42:43], v[42:43], v[136:137]
	v_pk_mul_f32 v[38:39], v[38:39], v[148:149]
	v_pk_mul_f32 v[34:35], v[34:35], v[144:145]

.LBB0_677:
	s_nop 0
	v_max3_f32 v130, v82, v66, v83
	v_max3_f32 v131, v67, v84, v68
	v_max3_f32 v132, v97, v81, v97
	v_max3_f32 v130, v130, v85, v69
	v_max3_f32 v131, v131, v86, v70
	v_max3_f32 v130, v130, v87, v71
	v_max3_f32 v131, v131, v88, v72
	v_max3_f32 v130, v130, v89, v73
	v_max3_f32 v131, v131, v90, v74
	v_max3_f32 v130, v130, v91, v75
	v_max3_f32 v131, v131, v92, v76
	v_max3_f32 v130, v130, v93, v77
	v_max3_f32 v131, v131, v94, v78
	v_max3_f32 v130, v130, v95, v79
	v_max3_f32 v131, v131, v96, v80
	v_max3_f32 v130, v130, v131, v132
	v_mov_b32_e32 v131, v130
	s_nop 1
	v_permlane32_swap_b32_e32 v130, v131
	v_max3_f32 v130, v130, v131, v131
	v_cmp_lt_f32_e32 vcc, s39, v130
	s_cbranch_vccz .LBB0_681
	v_max3_f32 v130, v130, v163, v163
	v_exp_f32_e64 v131, -v130
	s_and_saveexec_b64 s[10:11], s[2:3]
	ds_write_b32 v174, v131
	s_or_b64 exec, exec, s[10:11]
	s_waitcnt lgkmcnt(0)
	ds_read_b128 v[132:135], v165 offset:64
	ds_read_b128 v[136:139], v165 offset:96
	ds_read_b128 v[140:143], v165
	ds_read_b128 v[144:147], v165 offset:32
	s_waitcnt lgkmcnt(0)
	v_pk_add_f32 v[82:83], v[82:83], v[130:131] op_sel_hi:[1,0] neg_lo:[0,1] neg_hi:[0,1]
	v_pk_add_f32 v[66:67], v[66:67], v[130:131] op_sel_hi:[1,0] neg_lo:[0,1] neg_hi:[0,1]
	v_pk_add_f32 v[84:85], v[84:85], v[130:131] op_sel_hi:[1,0] neg_lo:[0,1] neg_hi:[0,1]
	v_pk_add_f32 v[68:69], v[68:69], v[130:131] op_sel_hi:[1,0] neg_lo:[0,1] neg_hi:[0,1]
	v_pk_add_f32 v[86:87], v[86:87], v[130:131] op_sel_hi:[1,0] neg_lo:[0,1] neg_hi:[0,1]
	v_pk_add_f32 v[70:71], v[70:71], v[130:131] op_sel_hi:[1,0] neg_lo:[0,1] neg_hi:[0,1]
	v_pk_add_f32 v[88:89], v[88:89], v[130:131] op_sel_hi:[1,0] neg_lo:[0,1] neg_hi:[0,1]
	v_pk_add_f32 v[72:73], v[72:73], v[130:131] op_sel_hi:[1,0] neg_lo:[0,1] neg_hi:[0,1]
	v_pk_add_f32 v[90:91], v[90:91], v[130:131] op_sel_hi:[1,0] neg_lo:[0,1] neg_hi:[0,1]
	v_pk_add_f32 v[74:75], v[74:75], v[130:131] op_sel_hi:[1,0] neg_lo:[0,1] neg_hi:[0,1]
	v_pk_add_f32 v[92:93], v[92:93], v[130:131] op_sel_hi:[1,0] neg_lo:[0,1] neg_hi:[0,1]
	v_pk_add_f32 v[76:77], v[76:77], v[130:131] op_sel_hi:[1,0] neg_lo:[0,1] neg_hi:[0,1]
	v_pk_add_f32 v[94:95], v[94:95], v[130:131] op_sel_hi:[1,0] neg_lo:[0,1] neg_hi:[0,1]
	v_pk_add_f32 v[78:79], v[78:79], v[130:131] op_sel_hi:[1,0] neg_lo:[0,1] neg_hi:[0,1]
	v_pk_add_f32 v[96:97], v[96:97], v[130:131] op_sel_hi:[1,0] neg_lo:[0,1] neg_hi:[0,1]
	v_pk_add_f32 v[80:81], v[80:81], v[130:131] op_sel_hi:[1,0] neg_lo:[0,1] neg_hi:[0,1]
	v_mul_f32_e32 v175, v175, v131
	s_waitcnt lgkmcnt(2)
	v_pk_mul_f32 v[32:33], v[32:33], v[138:139]
	v_pk_mul_f32 v[28:29], v[28:29], v[134:135]
	s_waitcnt lgkmcnt(0)
	v_pk_mul_f32 v[24:25], v[24:25], v[146:147]
	v_pk_mul_f32 v[20:21], v[20:21], v[142:143]
	v_pk_mul_f32 v[30:31], v[30:31], v[136:137]
	v_pk_mul_f32 v[26:27], v[26:27], v[132:133]
	v_pk_mul_f32 v[22:23], v[22:23], v[144:145]
	v_pk_mul_f32 v[18:19], v[18:19], v[140:141]
	v_pk_mul_f32 v[16:17], v[16:17], v[138:139]
	v_pk_mul_f32 v[12:13], v[12:13], v[134:135]
	v_pk_mul_f32 v[8:9], v[8:9], v[146:147]
	v_pk_mul_f32 v[4:5], v[4:5], v[142:143]
	v_pk_mul_f32 v[14:15], v[14:15], v[136:137]
	v_pk_mul_f32 v[10:11], v[10:11], v[132:133]
	v_pk_mul_f32 v[6:7], v[6:7], v[144:145]
	v_pk_mul_f32 v[2:3], v[2:3], v[140:141]
